# FoX attention inner loop VALU trimming: V-fragment LDS addresses from two per-tile bases + immediate offsets (-30 VALU/tile), 32 scalar subs -> 16 packed subs, 9 pad nops between plain v_max ops remov
# speedup vs baseline: 1.0151x; 1.0025x over previous
; #define LAS __attribute__((address_space(3)))
; #define LDS_WAIT() asm volatile("s_waitcnt lgkmcnt(0)" ::: "memory")
; __device__ __forceinline__ float max3f(float a, float b, float c) { float r; asm("v_max3_f32 %0, %1, %2, %3" : "=v"(r) : "v"(a), "v"(b), "v"(c)); return r; }
; __device__ __forceinline__ float rowmax32(const f32x16& p0, const f32x16& p1) {
;     float a = max3f(p0[0], p0[1], p1[0]), b = max3f(p0[2], p0[3], p1[1]); a = max3f(a, p1[2], p1[3]);
; #pragma unroll
;     for (int r = 4; r < 16; r += 4) { a = max3f(a, p0[r], p0[r + 1]); b = max3f(b, p0[r + 2], p0[r + 3]); a = max3f(a, p1[r], p1[r + 1]); b = max3f(b, p1[r + 2], p1[r + 3]); }
;     return max2f(a, b);
; }
; __device__ __forceinline__ float rowmax16(const f32x16& p0) {
;     float a = max3f(p0[0], p0[1], p0[2]), b = max3f(p0[3], p0[4], p0[5]);
;     a = max3f(a, p0[6], p0[7]); b = max3f(b, p0[8], p0[9]); a = max3f(a, p0[10], p0[11]); b = max3f(b, p0[12], p0[13]); a = max3f(a, p0[14], p0[15]);
;     return max2f(a, b);
; }
; __device__ __forceinline__ float pswap_max(float m) { auto rr = __builtin_amdgcn_permlane32_swap(__float_as_uint(m), __float_as_uint(m), false, false); return max2f(__uint_as_float(rr[0]), __uint_as_float(rr[1])); }
; __device__ __forceinline__ void rescale_o(f32x16 (&o)[2], float alpha, LAS float* wsf, int r32, int hi) {
;     if (hi == 0) wsf[r32] = alpha;
;     LDS_WAIT(); asm volatile("" ::: "memory");
; #pragma unroll
;     for (int j = 0; j < 4; ++j) { const f32x4 a = *(const LAS f32x4*)(wsf + 8 * j + 4 * hi);
; #pragma unroll
;         for (int e = 0; e < 4; ++e) { o[0][4 * j + e] *= a[e]; o[1][4 * j + e] *= a[e]; } }
;     LDS_WAIT(); asm volatile("" ::: "memory");
; }
; __device__ __forceinline__ void fox_softmax(f32x16& p0, f32x16& p1, f32x16 (&o)[2], float& mrun, float& lrun, int kv0, int qtok, bool diag, LAS float* wsf, int r32, int hi) {
;     if (__builtin_amdgcn_readfirstlane((int)diag)) {
; #pragma unroll
;         for (int r = 0; r < 16; ++r) { const int kv = kv0 + (r & 3) + 8 * (r >> 2); if (kv > qtok) p0[r] = -INFINITY; if (kv + 32 > qtok) p1[r] = -INFINITY; } }
;     float mt = pswap_max(rowmax32(p0, p1));
;     if (__any(mt > mrun + RESC_THR)) { const float mnew = max2f(mrun, mt), alpha = __builtin_amdgcn_exp2f(mrun - mnew); mrun = mnew; lrun *= alpha; rescale_o(o, alpha, wsf, r32, hi); }
.LBB0_428:
	v_max3_f32 v96, v80, v81, v32
	v_max3_f32 v98, v82, v83, v33
	v_max3_f32 v96, v96, v34, v35
	v_max3_f32 v98, v98, v86, v87
	v_max3_f32 v96, v96, v84, v85
	v_max3_f32 v98, v98, v38, v39
	v_max3_f32 v96, v96, v36, v37
	v_max3_f32 v98, v98, v90, v91
	v_max3_f32 v96, v96, v88, v89
	v_max3_f32 v98, v98, v42, v43
	v_max3_f32 v96, v96, v40, v41
	v_max3_f32 v98, v98, v94, v95
	v_max3_f32 v96, v96, v92, v93
	v_max3_f32 v98, v98, v46, v47
	v_max3_f32 v96, v96, v44, v45
	v_max_f32_e32 v96, v96, v98
	v_mov_b32_e32 v98, v96
	s_nop 1
	v_permlane32_swap_b32_e32 v96, v98
	v_max_f32_e32 v96, v96, v98
	v_add_f32_e32 v98, 0x41000000, v214
	v_cmp_gt_f32_e32 vcc, v96, v98
	s_cbranch_vccz .LBB0_432
	v_max_f32_e32 v96, v214, v96
	s_nop 0
	v_sub_f32_e32 v98, v214, v96
	v_exp_f32_e32 v98, v98
	s_and_saveexec_b64 s[6:7], s[4:5]
	ds_write_b32 v165, v98
	s_or_b64 exec, exec, s[6:7]
	s_waitcnt lgkmcnt(0)
	v_add_u32_e32 v99, s86, v166
	ds_read_b128 v[218:221], v99 offset:96
	ds_read_b128 v[222:225], v99 offset:64
	ds_read_b128 v[226:229], v99 offset:32
	ds_read_b128 v[230:233], v99
	s_waitcnt lgkmcnt(0)
	v_mul_f32_e32 v149, v149, v98
	s_waitcnt lgkmcnt(3)
	v_pk_mul_f32 v[28:29], v[28:29], v[218:219]
	s_waitcnt lgkmcnt(2)
	v_pk_mul_f32 v[24:25], v[24:25], v[222:223]
	s_waitcnt lgkmcnt(1)
	v_pk_mul_f32 v[20:21], v[20:21], v[226:227]
	v_pk_mul_f32 v[30:31], v[30:31], v[220:221]
	v_pk_mul_f32 v[26:27], v[26:27], v[224:225]
	v_pk_mul_f32 v[22:23], v[22:23], v[228:229]
	s_waitcnt lgkmcnt(0)
	v_pk_mul_f32 v[18:19], v[18:19], v[232:233]
	v_pk_mul_f32 v[16:17], v[16:17], v[230:231]
	v_pk_mul_f32 v[12:13], v[12:13], v[218:219]
	v_pk_mul_f32 v[8:9], v[8:9], v[222:223]
	v_pk_mul_f32 v[4:5], v[4:5], v[226:227]
	v_pk_mul_f32 v[14:15], v[14:15], v[220:221]
	v_pk_mul_f32 v[10:11], v[10:11], v[224:225]
	v_pk_mul_f32 v[6:7], v[6:7], v[228:229]
	v_pk_mul_f32 v[2:3], v[2:3], v[232:233]
	v_pk_mul_f32 v[0:1], v[0:1], v[230:231]
	v_mov_b32_e32 v214, v96
; #define LAS __attribute__((address_space(3)))
; __device__ __forceinline__ s16x4 vtr(const LAS unsigned char* p) { return __builtin_bit_cast(s16x4, __builtin_amdgcn_ds_read_tr16_b64_v4i16((LAS v4i16_t*)p)); }
; template <int DHS>
; __device__ __forceinline__ void pv_step(f32x16 (&o)[2], const LAS unsigned char* vb, int vsw, int s, bf16x8 pa) {
; #pragma unroll
;     for (int d0 = 0; d0 < 2; ++d0) {
;         const s16x4 lo = vtr(vb + d0 * (DHS + vsw) + s * 1024), hi = vtr(vb + d0 * (DHS + vsw) + s * 1024 + 512);
;         const bf16x8 vf = (bf16x8){lo[0], lo[1], lo[2], lo[3], hi[0], hi[1], hi[2], hi[3]};
;         o[d0] = __builtin_amdgcn_mfma_f32_32x32x16_bf16(pa, vf, o[d0], 0, 0, 0);
;     }
; }
; __device__ __forceinline__ void fox_softmax(f32x16& p0, f32x16& p1, f32x16 (&o)[2], float& mrun, float& lrun, int kv0, int qtok, bool diag, LAS float* wsf, int r32, int hi) {
;     ...
;     float rs = 0.f;
; #pragma unroll
;     for (int r = 0; r < 16; ++r) { p0[r] = __builtin_amdgcn_exp2f(p0[r] - mrun); p1[r] = __builtin_amdgcn_exp2f(p1[r] - mrun); rs += p0[r] + p1[r]; }
;     lrun += rs;
.LBB0_432:
	v_pk_add_f32 v[32:33], v[32:33], v[214:215] op_sel:[0,0] op_sel_hi:[1,0] neg_lo:[0,1] neg_hi:[0,1]
	v_pk_add_f32 v[34:35], v[34:35], v[214:215] op_sel:[0,0] op_sel_hi:[1,0] neg_lo:[0,1] neg_hi:[0,1]
	v_pk_add_f32 v[36:37], v[36:37], v[214:215] op_sel:[0,0] op_sel_hi:[1,0] neg_lo:[0,1] neg_hi:[0,1]
	v_pk_add_f32 v[38:39], v[38:39], v[214:215] op_sel:[0,0] op_sel_hi:[1,0] neg_lo:[0,1] neg_hi:[0,1]
	v_pk_add_f32 v[40:41], v[40:41], v[214:215] op_sel:[0,0] op_sel_hi:[1,0] neg_lo:[0,1] neg_hi:[0,1]
	v_pk_add_f32 v[42:43], v[42:43], v[214:215] op_sel:[0,0] op_sel_hi:[1,0] neg_lo:[0,1] neg_hi:[0,1]
	v_pk_add_f32 v[44:45], v[44:45], v[214:215] op_sel:[0,0] op_sel_hi:[1,0] neg_lo:[0,1] neg_hi:[0,1]
	v_pk_add_f32 v[46:47], v[46:47], v[214:215] op_sel:[0,0] op_sel_hi:[1,0] neg_lo:[0,1] neg_hi:[0,1]
	v_pk_add_f32 v[80:81], v[80:81], v[214:215] op_sel:[0,0] op_sel_hi:[1,0] neg_lo:[0,1] neg_hi:[0,1]
	v_pk_add_f32 v[82:83], v[82:83], v[214:215] op_sel:[0,0] op_sel_hi:[1,0] neg_lo:[0,1] neg_hi:[0,1]
	v_pk_add_f32 v[84:85], v[84:85], v[214:215] op_sel:[0,0] op_sel_hi:[1,0] neg_lo:[0,1] neg_hi:[0,1]
	v_pk_add_f32 v[86:87], v[86:87], v[214:215] op_sel:[0,0] op_sel_hi:[1,0] neg_lo:[0,1] neg_hi:[0,1]
	v_pk_add_f32 v[88:89], v[88:89], v[214:215] op_sel:[0,0] op_sel_hi:[1,0] neg_lo:[0,1] neg_hi:[0,1]
	v_pk_add_f32 v[90:91], v[90:91], v[214:215] op_sel:[0,0] op_sel_hi:[1,0] neg_lo:[0,1] neg_hi:[0,1]
	v_pk_add_f32 v[92:93], v[92:93], v[214:215] op_sel:[0,0] op_sel_hi:[1,0] neg_lo:[0,1] neg_hi:[0,1]
	v_pk_add_f32 v[94:95], v[94:95], v[214:215] op_sel:[0,0] op_sel_hi:[1,0] neg_lo:[0,1] neg_hi:[0,1]
	v_exp_f32_e32 v217, v32
	v_exp_f32_e32 v215, v80
	v_exp_f32_e32 v96, v81
	v_exp_f32_e32 v80, v33
	v_add_f32_e32 v81, v217, v215
	s_mul_hi_u32 s6, s47, 0xaaaaaaab
	s_lshr_b32 s6, s6, 1
	v_pk_add_f32 v[32:33], v[80:81], v[96:97]
	s_mul_i32 s6, s6, 0xc000
	s_sub_i32 s100, s60, s6
	v_add3_u32 v241, s100, v201, v186
	v_add3_u32 v242, s100, v193, v186
	v_pk_add_f32 v[98:99], v[32:33], v[32:33] op_sel_hi:[0,1]
	v_exp_f32_e32 v81, v82
	v_exp_f32_e32 v226, v34
	v_exp_f32_e32 v98, v83
	v_exp_f32_e32 v82, v35
	v_add_f32_e32 v83, v226, v81
	v_pk_add_f32 v[32:33], v[82:83], v[98:99]
	v_pk_add_f32 v[34:35], v[32:33], v[32:33] op_sel_hi:[0,1]
	v_exp_f32_e32 v83, v84
	v_exp_f32_e32 v99, v36
	v_exp_f32_e32 v34, v85
	v_exp_f32_e32 v84, v37
	v_add_f32_e32 v85, v99, v83
	v_pk_add_f32 v[32:33], v[84:85], v[34:35]
	v_cvt_pk_bf16_f32 v34, v83, v34
	v_pk_add_f32 v[36:37], v[32:33], v[32:33] op_sel_hi:[0,1]
	v_exp_f32_e32 v35, v86
	v_exp_f32_e32 v85, v38
	v_exp_f32_e32 v36, v87
	v_exp_f32_e32 v86, v39
	v_add_f32_e32 v87, v85, v35
	v_cvt_pk_bf16_f32 v35, v35, v36
	v_pk_add_f32 v[32:33], v[86:87], v[36:37]
	v_pk_add_f32 v[218:219], v[32:33], v[32:33] op_sel_hi:[0,1]
	v_exp_f32_e32 v87, v88
	v_exp_f32_e32 v233, v40
	v_exp_f32_e32 v218, v89
	v_exp_f32_e32 v88, v41
	v_add_f32_e32 v89, v233, v87
	v_pk_add_f32 v[32:33], v[88:89], v[218:219]
	ds_read_b64_tr_b16 v[36:37], v241
	ds_read_b64_tr_b16 v[38:39], v241 offset:512
	v_pk_add_f32 v[220:221], v[32:33], v[32:33] op_sel_hi:[0,1]
	v_exp_f32_e32 v89, v90
	v_exp_f32_e32 v219, v42
	v_exp_f32_e32 v220, v91
	v_exp_f32_e32 v90, v43
	v_add_f32_e32 v91, v219, v89
	v_pk_add_f32 v[32:33], v[90:91], v[220:221]
	ds_read_b64_tr_b16 v[40:41], v242
	ds_read_b64_tr_b16 v[42:43], v242 offset:512
	v_pk_add_f32 v[222:223], v[32:33], v[32:33] op_sel_hi:[0,1]
	v_exp_f32_e32 v91, v92
	v_exp_f32_e32 v221, v44
	v_exp_f32_e32 v222, v93
	v_exp_f32_e32 v44, v45
	v_add_f32_e32 v45, v221, v91
	v_pk_add_f32 v[32:33], v[44:45], v[222:223]
	v_pk_add_f32 v[92:93], v[32:33], v[32:33] op_sel_hi:[0,1]
	v_cvt_pk_bf16_f32 v32, v215, v96
	v_cvt_pk_bf16_f32 v33, v81, v98
	v_exp_f32_e32 v45, v94
	s_waitcnt lgkmcnt(2)
	v_mfma_f32_32x32x16_bf16 v[16:31], v[32:35], v[36:39], v[16:31]
	v_exp_f32_e32 v92, v95
	v_cvt_pk_bf16_f32 v36, v87, v218
	v_cvt_pk_bf16_f32 v37, v89, v220
	v_cvt_pk_bf16_f32 v38, v91, v222
	v_cvt_pk_bf16_f32 v39, v45, v92
	s_waitcnt lgkmcnt(0)
	v_mfma_f32_32x32x16_bf16 v[0:15], v[32:35], v[40:43], v[0:15]
	ds_read_b64_tr_b16 v[32:33], v241 offset:1024
	ds_read_b64_tr_b16 v[34:35], v241 offset:1536
	ds_read_b64_tr_b16 v[40:41], v242 offset:1024
	ds_read_b64_tr_b16 v[42:43], v242 offset:1536
	s_waitcnt lgkmcnt(2)
	v_mfma_f32_32x32x16_bf16 v[16:31], v[36:39], v[32:35], v[16:31]
	v_cvt_pk_bf16_f32 v32, v217, v80
	v_cvt_pk_bf16_f32 v33, v226, v82
	v_cvt_pk_bf16_f32 v34, v99, v84
	v_cvt_pk_bf16_f32 v35, v85, v86
	v_exp_f32_e32 v80, v46
	s_waitcnt lgkmcnt(0)
	v_mfma_f32_32x32x16_bf16 v[0:15], v[36:39], v[40:43], v[0:15]
	ds_read_b64_tr_b16 v[36:37], v241 offset:2048
	ds_read_b64_tr_b16 v[38:39], v241 offset:2560
	ds_read_b64_tr_b16 v[40:41], v242 offset:2048
	ds_read_b64_tr_b16 v[42:43], v242 offset:2560
	s_waitcnt lgkmcnt(2)
	v_mfma_f32_32x32x16_bf16 v[16:31], v[32:35], v[36:39], v[16:31]
	v_exp_f32_e32 v46, v47
	v_cvt_pk_bf16_f32 v36, v233, v88
	v_cvt_pk_bf16_f32 v37, v219, v90
	v_cvt_pk_bf16_f32 v38, v221, v44
	s_waitcnt lgkmcnt(0)
	v_mfma_f32_32x32x16_bf16 v[0:15], v[32:35], v[40:43], v[0:15]
	v_cvt_pk_bf16_f32 v39, v80, v46
	ds_read_b64_tr_b16 v[32:33], v241 offset:3072
	ds_read_b64_tr_b16 v[34:35], v241 offset:3584
	ds_read_b64_tr_b16 v[40:41], v242 offset:3072
	ds_read_b64_tr_b16 v[42:43], v242 offset:3584
	s_waitcnt lgkmcnt(2)
	v_mfma_f32_32x32x16_bf16 v[16:31], v[36:39], v[32:35], v[16:31]
	v_add_f32_e32 v47, v80, v45
	v_add_f32_e64 v32, v46, v92
	v_add_f32_e64 v33, v47, v93
	v_add_f32_e32 v32, v32, v33
	v_add_f32_e32 v149, v149, v32
	s_waitcnt lgkmcnt(0)
	v_mfma_f32_32x32x16_bf16 v[0:15], v[36:39], v[40:43], v[0:15]
	s_andn2_b64 vcc, exec, s[42:43]
	s_cbranch_vccz .LBB0_420
	s_branch .LBB0_421

; #define LAS __attribute__((address_space(3)))
; #define LDS_WAIT() asm volatile("s_waitcnt lgkmcnt(0)" ::: "memory")
; __device__ __forceinline__ float max3f(float a, float b, float c) { float r; asm("v_max3_f32 %0, %1, %2, %3" : "=v"(r) : "v"(a), "v"(b), "v"(c)); return r; }
; __device__ __forceinline__ float rowmax32(const f32x16& p0, const f32x16& p1) {
;     float a = max3f(p0[0], p0[1], p1[0]), b = max3f(p0[2], p0[3], p1[1]); a = max3f(a, p1[2], p1[3]);
; #pragma unroll
;     for (int r = 4; r < 16; r += 4) { a = max3f(a, p0[r], p0[r + 1]); b = max3f(b, p0[r + 2], p0[r + 3]); a = max3f(a, p1[r], p1[r + 1]); b = max3f(b, p1[r + 2], p1[r + 3]); }
;     return max2f(a, b);
; }
; __device__ __forceinline__ float rowmax16(const f32x16& p0) {
;     float a = max3f(p0[0], p0[1], p0[2]), b = max3f(p0[3], p0[4], p0[5]);
;     a = max3f(a, p0[6], p0[7]); b = max3f(b, p0[8], p0[9]); a = max3f(a, p0[10], p0[11]); b = max3f(b, p0[12], p0[13]); a = max3f(a, p0[14], p0[15]);
;     return max2f(a, b);
; }
; __device__ __forceinline__ float pswap_max(float m) { auto rr = __builtin_amdgcn_permlane32_swap(__float_as_uint(m), __float_as_uint(m), false, false); return max2f(__uint_as_float(rr[0]), __uint_as_float(rr[1])); }
; __device__ __forceinline__ void rescale_o(f32x16 (&o)[2], float alpha, LAS float* wsf, int r32, int hi) {
;     if (hi == 0) wsf[r32] = alpha;
;     LDS_WAIT(); asm volatile("" ::: "memory");
; #pragma unroll
;     for (int j = 0; j < 4; ++j) { const f32x4 a = *(const LAS f32x4*)(wsf + 8 * j + 4 * hi);
; #pragma unroll
;         for (int e = 0; e < 4; ++e) { o[0][4 * j + e] *= a[e]; o[1][4 * j + e] *= a[e]; } }
;     LDS_WAIT(); asm volatile("" ::: "memory");
; }
; __device__ __forceinline__ void fox_softmax(f32x16& p0, f32x16& p1, f32x16 (&o)[2], float& mrun, float& lrun, int kv0, int qtok, bool diag, LAS float* wsf, int r32, int hi) {
;     if (__builtin_amdgcn_readfirstlane((int)diag)) {
; #pragma unroll
;         for (int r = 0; r < 16; ++r) { const int kv = kv0 + (r & 3) + 8 * (r >> 2); if (kv > qtok) p0[r] = -INFINITY; if (kv + 32 > qtok) p1[r] = -INFINITY; } }
;     float mt = pswap_max(rowmax32(p0, p1));
;     if (__any(mt > mrun + RESC_THR)) { const float mnew = max2f(mrun, mt), alpha = __builtin_amdgcn_exp2f(mrun - mnew); mrun = mnew; lrun *= alpha; rescale_o(o, alpha, wsf, r32, hi); }
.LBB0_1338:
	v_max3_f32 v96, v80, v81, v32
	v_max3_f32 v98, v82, v83, v33
	v_max3_f32 v96, v96, v34, v35
	v_max3_f32 v98, v98, v86, v87
	v_max3_f32 v96, v96, v84, v85
	v_max3_f32 v98, v98, v38, v39
	v_max3_f32 v96, v96, v36, v37
	v_max3_f32 v98, v98, v90, v91
	v_max3_f32 v96, v96, v88, v89
	v_max3_f32 v98, v98, v42, v43
	v_max3_f32 v96, v96, v40, v41
	v_max3_f32 v98, v98, v94, v95
	v_max3_f32 v96, v96, v92, v93
	v_max3_f32 v98, v98, v46, v47
	v_max3_f32 v96, v96, v44, v45
	v_max_f32_e32 v96, v96, v98
	v_mov_b32_e32 v98, v96
	s_nop 1
	v_permlane32_swap_b32_e32 v96, v98
	v_max_f32_e32 v96, v96, v98
	v_add_f32_e32 v98, 0x41000000, v214
	v_cmp_gt_f32_e32 vcc, v96, v98
	s_cbranch_vccz .LBB0_1342
	v_max_f32_e32 v96, v214, v96
	s_nop 0
	v_sub_f32_e32 v98, v214, v96
	v_exp_f32_e32 v98, v98
	s_and_saveexec_b64 s[6:7], s[4:5]
	ds_write_b32 v165, v98
	s_or_b64 exec, exec, s[6:7]
	s_waitcnt lgkmcnt(0)
	v_add_u32_e32 v99, s82, v166
	ds_read_b128 v[218:221], v99 offset:96
	ds_read_b128 v[222:225], v99 offset:64
	ds_read_b128 v[226:229], v99 offset:32
	ds_read_b128 v[230:233], v99
	s_waitcnt lgkmcnt(0)
	v_mul_f32_e32 v149, v149, v98
	s_waitcnt lgkmcnt(3)
	v_pk_mul_f32 v[28:29], v[28:29], v[218:219]
	s_waitcnt lgkmcnt(2)
	v_pk_mul_f32 v[24:25], v[24:25], v[222:223]
	s_waitcnt lgkmcnt(1)
	v_pk_mul_f32 v[20:21], v[20:21], v[226:227]
	v_pk_mul_f32 v[30:31], v[30:31], v[220:221]
	v_pk_mul_f32 v[26:27], v[26:27], v[224:225]
	v_pk_mul_f32 v[22:23], v[22:23], v[228:229]
	s_waitcnt lgkmcnt(0)
	v_pk_mul_f32 v[18:19], v[18:19], v[232:233]
	v_pk_mul_f32 v[16:17], v[16:17], v[230:231]
	v_pk_mul_f32 v[12:13], v[12:13], v[218:219]
	v_pk_mul_f32 v[8:9], v[8:9], v[222:223]
	v_pk_mul_f32 v[4:5], v[4:5], v[226:227]
	v_pk_mul_f32 v[14:15], v[14:15], v[220:221]
	v_pk_mul_f32 v[10:11], v[10:11], v[224:225]
	v_pk_mul_f32 v[6:7], v[6:7], v[228:229]
	v_pk_mul_f32 v[2:3], v[2:3], v[232:233]
	v_pk_mul_f32 v[0:1], v[0:1], v[230:231]
	v_mov_b32_e32 v214, v96
